# speedup vs baseline: 1.0403x; 1.0403x over previous
_Z13logits_kernelPKDv8_DF16bS1_PKfS3_PDv2_fS5_Pf:
	s_load_dwordx4 s[4:7], s[0:1], 0x0
	s_load_dwordx4 s[12:15], s[0:1], 0x10
	s_load_dwordx4 s[24:27], s[0:1], 0x20
	s_load_dwordx2 s[28:29], s[0:1], 0x30
	s_and_b32 s3, s2, 7
	s_lshl_b32 s3, s3, 1
	s_bfe_u32 s8, s2, 0x10003
	s_lshr_b32 s10, s2, 4
	s_or_b32 s3, s3, s8
	v_lshrrev_b32_e32 v1, 6, v0
	v_and_b32_e32 v2, 63, v0
	s_movk_i32 s11, 0x3000
	v_lshlrev_b32_e32 v2, 4, v2
	v_and_b32_e32 v5, 31, v0
	v_mad_u32_u24 v2, v1, s11, v2
	v_lshlrev_b32_e32 v5, 2, v5
	s_lshl_b32 s9, s3, 9
	v_add_u32_e32 v3, 0x1000, v2
	v_add_u32_e32 v4, 0x2000, v2
	v_add_u32_e32 v5, s9, v5
	s_mul_i32 s8, s10, 0xc000
	s_mul_i32 s9, s3, 0x30000
	s_waitcnt lgkmcnt(0)
	s_load_dword s22, s[14:15], 0x0
	global_load_dword v248, v5, s[12:13]
	global_load_dword v249, v5, s[12:13] offset:128
	global_load_dword v250, v5, s[12:13] offset:256
	global_load_dword v251, v5, s[12:13] offset:384
	s_add_u32 s4, s4, s8
	s_addc_u32 s5, s5, 0
	s_add_u32 s6, s6, s9
	s_addc_u32 s7, s7, 0
	s_add_u32 s16, s6, 0xc000
	s_addc_u32 s17, s7, 0
	s_add_u32 s18, s6, 0x18000
	s_addc_u32 s19, s7, 0
	s_add_u32 s20, s6, 0x24000
	s_addc_u32 s21, s7, 0
	global_load_dwordx4 v[8:11], v2, s[4:5]
	global_load_dwordx4 v[56:59], v2, s[6:7]
	global_load_dwordx4 v[104:107], v2, s[16:17]
	global_load_dwordx4 v[152:155], v2, s[18:19]
	global_load_dwordx4 v[200:203], v2, s[20:21]
	global_load_dwordx4 v[12:15], v2, s[4:5] offset:1024
	global_load_dwordx4 v[60:63], v2, s[6:7] offset:1024
	global_load_dwordx4 v[108:111], v2, s[16:17] offset:1024
	global_load_dwordx4 v[156:159], v2, s[18:19] offset:1024
	global_load_dwordx4 v[204:207], v2, s[20:21] offset:1024
	global_load_dwordx4 v[16:19], v2, s[4:5] offset:2048
	global_load_dwordx4 v[64:67], v2, s[6:7] offset:2048
	global_load_dwordx4 v[112:115], v2, s[16:17] offset:2048
	global_load_dwordx4 v[160:163], v2, s[18:19] offset:2048
	global_load_dwordx4 v[208:211], v2, s[20:21] offset:2048
	global_load_dwordx4 v[20:23], v2, s[4:5] offset:3072
	global_load_dwordx4 v[68:71], v2, s[6:7] offset:3072
	global_load_dwordx4 v[116:119], v2, s[16:17] offset:3072
	global_load_dwordx4 v[164:167], v2, s[18:19] offset:3072
	global_load_dwordx4 v[212:215], v2, s[20:21] offset:3072
	global_load_dwordx4 v[24:27], v3, s[4:5]
	global_load_dwordx4 v[72:75], v3, s[6:7]
	global_load_dwordx4 v[120:123], v3, s[16:17]
	global_load_dwordx4 v[168:171], v3, s[18:19]
	global_load_dwordx4 v[216:219], v3, s[20:21]
	global_load_dwordx4 v[28:31], v3, s[4:5] offset:1024
	global_load_dwordx4 v[76:79], v3, s[6:7] offset:1024
	global_load_dwordx4 v[124:127], v3, s[16:17] offset:1024
	global_load_dwordx4 v[172:175], v3, s[18:19] offset:1024
	global_load_dwordx4 v[220:223], v3, s[20:21] offset:1024
	global_load_dwordx4 v[32:35], v3, s[4:5] offset:2048
	global_load_dwordx4 v[80:83], v3, s[6:7] offset:2048
	global_load_dwordx4 v[128:131], v3, s[16:17] offset:2048
	global_load_dwordx4 v[176:179], v3, s[18:19] offset:2048
	global_load_dwordx4 v[224:227], v3, s[20:21] offset:2048
	global_load_dwordx4 v[36:39], v3, s[4:5] offset:3072
	global_load_dwordx4 v[84:87], v3, s[6:7] offset:3072
	global_load_dwordx4 v[132:135], v3, s[16:17] offset:3072
	global_load_dwordx4 v[180:183], v3, s[18:19] offset:3072
	global_load_dwordx4 v[228:231], v3, s[20:21] offset:3072
	global_load_dwordx4 v[40:43], v4, s[4:5]
	global_load_dwordx4 v[88:91], v4, s[6:7]
	global_load_dwordx4 v[136:139], v4, s[16:17]
	global_load_dwordx4 v[184:187], v4, s[18:19]
	global_load_dwordx4 v[232:235], v4, s[20:21]
	global_load_dwordx4 v[44:47], v4, s[4:5] offset:1024
	global_load_dwordx4 v[92:95], v4, s[6:7] offset:1024
	global_load_dwordx4 v[140:143], v4, s[16:17] offset:1024
	global_load_dwordx4 v[188:191], v4, s[18:19] offset:1024
	global_load_dwordx4 v[236:239], v4, s[20:21] offset:1024
	global_load_dwordx4 v[48:51], v4, s[4:5] offset:2048
	global_load_dwordx4 v[96:99], v4, s[6:7] offset:2048
	global_load_dwordx4 v[144:147], v4, s[16:17] offset:2048
	global_load_dwordx4 v[192:195], v4, s[18:19] offset:2048
	global_load_dwordx4 v[240:243], v4, s[20:21] offset:2048
	global_load_dwordx4 v[52:55], v4, s[4:5] offset:3072
	global_load_dwordx4 v[100:103], v4, s[6:7] offset:3072
	global_load_dwordx4 v[148:151], v4, s[16:17] offset:3072
	global_load_dwordx4 v[196:199], v4, s[18:19] offset:3072
	global_load_dwordx4 v[244:247], v4, s[20:21] offset:3072
	s_waitcnt vmcnt(58)
	v_mfma_f32_32x32x16_bf16 a[0:15], v[8:11], v[56:59], 0
	s_waitcnt vmcnt(57)
	v_mfma_f32_32x32x16_bf16 a[0:15], v[8:11], v[104:107], a[0:15]
	s_waitcnt vmcnt(56)
	v_mfma_f32_32x32x16_bf16 a[0:15], v[8:11], v[152:155], a[0:15]
	s_waitcnt vmcnt(55)
	v_mfma_f32_32x32x16_bf16 a[0:15], v[8:11], v[200:203], a[0:15]
	s_waitcnt vmcnt(53)
	v_mfma_f32_32x32x16_bf16 a[0:15], v[12:15], v[60:63], a[0:15]
	s_waitcnt vmcnt(52)
	v_mfma_f32_32x32x16_bf16 a[0:15], v[12:15], v[108:111], a[0:15]
	s_waitcnt vmcnt(51)
	v_mfma_f32_32x32x16_bf16 a[0:15], v[12:15], v[156:159], a[0:15]
	s_waitcnt vmcnt(50)
	v_mfma_f32_32x32x16_bf16 a[0:15], v[12:15], v[204:207], a[0:15]
	s_waitcnt vmcnt(48)
	v_mfma_f32_32x32x16_bf16 a[0:15], v[16:19], v[64:67], a[0:15]
	s_waitcnt vmcnt(47)
	v_mfma_f32_32x32x16_bf16 a[0:15], v[16:19], v[112:115], a[0:15]
	s_waitcnt vmcnt(46)
	v_mfma_f32_32x32x16_bf16 a[0:15], v[16:19], v[160:163], a[0:15]
	s_waitcnt vmcnt(45)
	v_mfma_f32_32x32x16_bf16 a[0:15], v[16:19], v[208:211], a[0:15]
	s_waitcnt vmcnt(43)
	v_mfma_f32_32x32x16_bf16 a[0:15], v[20:23], v[68:71], a[0:15]
	s_waitcnt vmcnt(42)
	v_mfma_f32_32x32x16_bf16 a[0:15], v[20:23], v[116:119], a[0:15]
	s_waitcnt vmcnt(41)
	v_mfma_f32_32x32x16_bf16 a[0:15], v[20:23], v[164:167], a[0:15]
	s_waitcnt vmcnt(40)
	v_mfma_f32_32x32x16_bf16 a[0:15], v[20:23], v[212:215], a[0:15]
	s_waitcnt vmcnt(38)
	v_mfma_f32_32x32x16_bf16 a[0:15], v[24:27], v[72:75], a[0:15]
	s_waitcnt vmcnt(37)
	v_mfma_f32_32x32x16_bf16 a[0:15], v[24:27], v[120:123], a[0:15]
	s_waitcnt vmcnt(36)
	v_mfma_f32_32x32x16_bf16 a[0:15], v[24:27], v[168:171], a[0:15]
	s_waitcnt vmcnt(35)
	v_mfma_f32_32x32x16_bf16 a[0:15], v[24:27], v[216:219], a[0:15]
	s_waitcnt vmcnt(33)
	v_mfma_f32_32x32x16_bf16 a[0:15], v[28:31], v[76:79], a[0:15]
	s_waitcnt vmcnt(32)
	v_mfma_f32_32x32x16_bf16 a[0:15], v[28:31], v[124:127], a[0:15]
	s_waitcnt vmcnt(31)
	v_mfma_f32_32x32x16_bf16 a[0:15], v[28:31], v[172:175], a[0:15]
	s_waitcnt vmcnt(30)
	v_mfma_f32_32x32x16_bf16 a[0:15], v[28:31], v[220:223], a[0:15]
	s_waitcnt vmcnt(28)
	v_mfma_f32_32x32x16_bf16 a[0:15], v[32:35], v[80:83], a[0:15]
	s_waitcnt vmcnt(27)
	v_mfma_f32_32x32x16_bf16 a[0:15], v[32:35], v[128:131], a[0:15]
	s_waitcnt vmcnt(26)
	v_mfma_f32_32x32x16_bf16 a[0:15], v[32:35], v[176:179], a[0:15]
	s_waitcnt vmcnt(25)
	v_mfma_f32_32x32x16_bf16 a[0:15], v[32:35], v[224:227], a[0:15]
	s_waitcnt vmcnt(23)
	v_mfma_f32_32x32x16_bf16 a[0:15], v[36:39], v[84:87], a[0:15]
	s_waitcnt vmcnt(22)
	v_mfma_f32_32x32x16_bf16 a[0:15], v[36:39], v[132:135], a[0:15]
	s_waitcnt vmcnt(21)
	v_mfma_f32_32x32x16_bf16 a[0:15], v[36:39], v[180:183], a[0:15]
	s_waitcnt vmcnt(20)
	v_mfma_f32_32x32x16_bf16 a[0:15], v[36:39], v[228:231], a[0:15]
	s_waitcnt vmcnt(18)
	v_mfma_f32_32x32x16_bf16 a[0:15], v[40:43], v[88:91], a[0:15]
	s_waitcnt vmcnt(17)
	v_mfma_f32_32x32x16_bf16 a[0:15], v[40:43], v[136:139], a[0:15]
	s_waitcnt vmcnt(16)
	v_mfma_f32_32x32x16_bf16 a[0:15], v[40:43], v[184:187], a[0:15]
	s_waitcnt vmcnt(15)
	v_mfma_f32_32x32x16_bf16 a[0:15], v[40:43], v[232:235], a[0:15]
	s_waitcnt vmcnt(13)
	v_mfma_f32_32x32x16_bf16 a[0:15], v[44:47], v[92:95], a[0:15]
	s_waitcnt vmcnt(12)
	v_mfma_f32_32x32x16_bf16 a[0:15], v[44:47], v[140:143], a[0:15]
	s_waitcnt vmcnt(11)
	v_mfma_f32_32x32x16_bf16 a[0:15], v[44:47], v[188:191], a[0:15]
	s_waitcnt vmcnt(10)
	v_mfma_f32_32x32x16_bf16 a[0:15], v[44:47], v[236:239], a[0:15]
	v_add_f32_e32 v8, 0, v248
	v_add_f32_e32 v8, v8, v249
	v_add_f32_e32 v8, v8, v250
	v_add_f32_e32 v8, v8, v251
	v_mov_b32_e32 v9, 0x3fb8aa3b
	s_waitcnt lgkmcnt(0)
	v_mul_f32_e32 v9, s22, v9
	v_exp_f32_e32 v9, v9
	v_add_f32_e32 v10, 0x2b8cbccc, v8
	v_div_scale_f32 v11, s[8:9], v10, v10, v9
	v_rcp_f32_e32 v12, v11
	v_div_scale_f32 v13, vcc, v9, v10, v9
	v_fma_f32 v14, -v11, v12, 1.0
	v_fmac_f32_e32 v12, v14, v12
	v_mul_f32_e32 v14, v13, v12
	v_fma_f32 v15, -v11, v14, v13
	v_fmac_f32_e32 v14, v15, v12
	v_fma_f32 v11, -v11, v14, v13
	v_div_fmas_f32 v11, v11, v12, v14
	v_div_fixup_f32 v9, v11, v10, v9
	v_lshlrev_b32_e32 v10, 2, v0
	v_add_u32_e32 v10, 0x4000, v10
	v_cmp_gt_u32_e32 vcc, 32, v0
	s_and_saveexec_b64 s[8:9], vcc
	ds_write2_b32 v10, v8, v9 offset0:128 offset1:160
	s_mov_b64 exec, s[8:9]
	s_waitcnt vmcnt(8)
	v_mfma_f32_32x32x16_bf16 a[0:15], v[48:51], v[96:99], a[0:15]
	s_waitcnt vmcnt(7)
	v_mfma_f32_32x32x16_bf16 a[0:15], v[48:51], v[144:147], a[0:15]
	s_waitcnt vmcnt(6)
	v_mfma_f32_32x32x16_bf16 a[0:15], v[48:51], v[192:195], a[0:15]
	s_waitcnt vmcnt(5)
	v_mfma_f32_32x32x16_bf16 a[0:15], v[48:51], v[240:243], a[0:15]
	v_mul_u32_u24_e32 v1, 0x1080, v1
	s_movk_i32 s4, 0x7f
	s_movk_i32 s6, 0x84
	v_cmp_lt_u32_e32 vcc, s4, v0
	v_lshrrev_b32_e32 v11, 3, v0
	v_and_b32_e32 v10, 31, v0
	v_and_b32_e32 v11, 4, v11
	v_mul_u32_u24_e32 v11, 0x84, v11
	v_lshlrev_b32_e32 v9, 2, v10
	v_bfe_u32 v6, v0, 2, 5
	v_and_b32_e32 v7, 3, v0
	v_add3_u32 v1, v1, v11, v9
	v_lshlrev_b32_e32 v8, 3, v7
	s_waitcnt vmcnt(3)
	v_mfma_f32_32x32x16_bf16 a[0:15], v[52:55], v[100:103], a[0:15]
	s_waitcnt vmcnt(2)
	v_mfma_f32_32x32x16_bf16 a[0:15], v[52:55], v[148:151], a[0:15]
	s_waitcnt vmcnt(1)
	v_mfma_f32_32x32x16_bf16 a[0:15], v[52:55], v[196:199], a[0:15]
	s_waitcnt vmcnt(0)
	v_mfma_f32_32x32x16_bf16 a[0:15], v[52:55], v[244:247], a[0:15]
	s_nop 11
	ds_write_b32 v1, a0
	ds_write_b32 v1, a1 offset:132
	ds_write_b32 v1, a2 offset:264
	ds_write_b32 v1, a3 offset:396
	ds_write_b32 v1, a4 offset:1056
	ds_write_b32 v1, a5 offset:1188
	ds_write_b32 v1, a6 offset:1320
	ds_write_b32 v1, a7 offset:1452
	ds_write_b32 v1, a8 offset:2112
	ds_write_b32 v1, a9 offset:2244
	ds_write_b32 v1, a10 offset:2376
	ds_write_b32 v1, a11 offset:2508
	ds_write_b32 v1, a12 offset:3168
	ds_write_b32 v1, a13 offset:3300
	ds_write_b32 v1, a14 offset:3432
	ds_write_b32 v1, a15 offset:3564
	v_bfe_u32 v6, v0, 2, 5
	v_and_b32_e32 v7, 3, v0
	v_lshlrev_b32_e32 v9, 3, v7
	v_readfirstlane_b32 s30, v0
	v_sub_u32_e32 v10, v6, v9
	s_waitcnt lgkmcnt(0)
	s_barrier
	s_cmpk_ge_u32 s30, 0x80
	s_cbranch_scc1 .Llg_k1
	v_mul_u32_u24_e32 v2, 0x84, v6
	v_lshlrev_b32_e32 v8, 5, v7
	v_add_u32_e32 v2, v2, v8
	v_add_u32_e32 v8, 0x4280, v8
	v_add_u32_e32 v3, 0x1080, v2
	v_add_u32_e32 v4, 0x2100, v2
	v_add_u32_e32 v5, 0x3180, v2
	ds_read_b128 v[48:51], v8
	ds_read_b128 v[52:55], v8 offset:16
	ds_read2_b32 v[16:17], v2 offset0:0 offset1:1
	ds_read2_b32 v[18:19], v2 offset0:2 offset1:3
	ds_read2_b32 v[20:21], v2 offset0:4 offset1:5
	ds_read2_b32 v[22:23], v2 offset0:6 offset1:7
	ds_read2_b32 v[24:25], v3 offset0:0 offset1:1
	ds_read2_b32 v[26:27], v3 offset0:2 offset1:3
	ds_read2_b32 v[28:29], v3 offset0:4 offset1:5
	ds_read2_b32 v[30:31], v3 offset0:6 offset1:7
	ds_read2_b32 v[32:33], v4 offset0:0 offset1:1
	ds_read2_b32 v[34:35], v4 offset0:2 offset1:3
	ds_read2_b32 v[36:37], v4 offset0:4 offset1:5
	ds_read2_b32 v[38:39], v4 offset0:6 offset1:7
	s_waitcnt lgkmcnt(4)
	ds_read2_b32 v[40:41], v5 offset0:0 offset1:1
	ds_read2_b32 v[42:43], v5 offset0:2 offset1:3
	ds_read2_b32 v[44:45], v5 offset0:4 offset1:5
	ds_read2_b32 v[46:47], v5 offset0:6 offset1:7
	s_waitcnt lgkmcnt(0)
	s_branch .Llg_join
